# cross-half row max / row sum exchanges by v_permlane32_swap instead of ds_bpermute (no LDS round trip), on top of the priority raise
# baseline (speedup 1.0000x reference)
.LBB0_471:
	v_cndmask_b32_e64 v70, v81, v226, s[78:79]
	v_max3_f32 v33, v18, v97, v20
	v_max3_f32 v33, v33, v19, v22
	v_max3_f32 v33, v33, v21, v24
	v_max3_f32 v33, v33, v23, v26
	v_max3_f32 v33, v33, v25, v28
	v_max3_f32 v33, v33, v27, v31
	v_max3_f32 v33, v33, v29, v30
	v_max3_f32 v33, v33, v32, v3
	v_max3_f32 v33, v33, v2, v5
	v_max3_f32 v33, v33, v4, v7
	v_max3_f32 v33, v33, v6, v9
	v_max3_f32 v33, v33, v8, v11
	v_max3_f32 v33, v33, v10, v13
	v_max3_f32 v33, v33, v12, v15
	v_max3_f32 v33, v33, v14, v17
	v_max3_f32 v33, v33, v16, v35
	v_max3_f32 v33, v33, v34, v37
	v_max3_f32 v33, v33, v36, v39
	v_max3_f32 v33, v33, v38, v41
	v_max3_f32 v33, v33, v40, v43
	v_max3_f32 v33, v33, v42, v45
	v_max3_f32 v33, v33, v44, v47
	v_max3_f32 v33, v33, v46, v49
	v_max3_f32 v33, v33, v48, v51
	v_max3_f32 v33, v33, v50, v53
	v_max3_f32 v33, v33, v52, v55
	v_max3_f32 v33, v33, v54, v57
	v_max3_f32 v33, v33, v56, v59
	v_max3_f32 v33, v33, v58, v61
	v_max3_f32 v33, v33, v60, v63
	v_max3_f32 v33, v33, v62, v65
	v_max3_f32 v33, v33, v64, v83
	v_max3_f32 v33, v33, v82, v85
	v_max3_f32 v33, v33, v84, v87
	v_max3_f32 v33, v33, v86, v89
	v_max3_f32 v33, v33, v88, v91
	v_max3_f32 v33, v33, v90, v93
	v_max3_f32 v33, v33, v92, v95
	v_max3_f32 v33, v33, v94, v70
	v_max_f32_e32 v33, v33, v96
	v_mov_b32_e32 v66, v33
	s_nop 1
	v_permlane32_swap_b32_e32 v66, v33
	s_nop 1
	v_max_f32_e32 v66, v33, v66
	v_pk_add_f32 v[2:3], v[2:3], v[66:67] op_sel_hi:[1,0] neg_lo:[0,1] neg_hi:[0,1]
	v_pk_add_f32 v[4:5], v[4:5], v[66:67] op_sel_hi:[1,0] neg_lo:[0,1] neg_hi:[0,1]
	v_pk_add_f32 v[6:7], v[6:7], v[66:67] op_sel_hi:[1,0] neg_lo:[0,1] neg_hi:[0,1]
	v_pk_add_f32 v[8:9], v[8:9], v[66:67] op_sel_hi:[1,0] neg_lo:[0,1] neg_hi:[0,1]
	v_pk_add_f32 v[10:11], v[10:11], v[66:67] op_sel_hi:[1,0] neg_lo:[0,1] neg_hi:[0,1]
	v_pk_add_f32 v[12:13], v[12:13], v[66:67] op_sel_hi:[1,0] neg_lo:[0,1] neg_hi:[0,1]
	v_pk_add_f32 v[14:15], v[14:15], v[66:67] op_sel_hi:[1,0] neg_lo:[0,1] neg_hi:[0,1]
	v_pk_add_f32 v[16:17], v[16:17], v[66:67] op_sel_hi:[1,0] neg_lo:[0,1] neg_hi:[0,1]
	v_pk_add_f32 v[18:19], v[18:19], v[66:67] op_sel_hi:[1,0] neg_lo:[0,1] neg_hi:[0,1]
	v_pk_add_f32 v[20:21], v[20:21], v[66:67] op_sel_hi:[1,0] neg_lo:[0,1] neg_hi:[0,1]
	v_pk_add_f32 v[22:23], v[22:23], v[66:67] op_sel_hi:[1,0] neg_lo:[0,1] neg_hi:[0,1]
	v_pk_add_f32 v[24:25], v[24:25], v[66:67] op_sel_hi:[1,0] neg_lo:[0,1] neg_hi:[0,1]
	v_pk_add_f32 v[26:27], v[26:27], v[66:67] op_sel_hi:[1,0] neg_lo:[0,1] neg_hi:[0,1]
	v_pk_add_f32 v[28:29], v[28:29], v[66:67] op_sel_hi:[1,0] neg_lo:[0,1] neg_hi:[0,1]
	v_pk_add_f32 v[30:31], v[30:31], v[66:67] op_sel_hi:[1,0] neg_lo:[0,1] neg_hi:[0,1]
	v_pk_add_f32 v[34:35], v[34:35], v[66:67] op_sel_hi:[1,0] neg_lo:[0,1] neg_hi:[0,1]
	v_pk_add_f32 v[36:37], v[36:37], v[66:67] op_sel_hi:[1,0] neg_lo:[0,1] neg_hi:[0,1]
	v_pk_add_f32 v[38:39], v[38:39], v[66:67] op_sel_hi:[1,0] neg_lo:[0,1] neg_hi:[0,1]
	v_pk_add_f32 v[40:41], v[40:41], v[66:67] op_sel_hi:[1,0] neg_lo:[0,1] neg_hi:[0,1]
	v_pk_add_f32 v[42:43], v[42:43], v[66:67] op_sel_hi:[1,0] neg_lo:[0,1] neg_hi:[0,1]
	v_pk_add_f32 v[44:45], v[44:45], v[66:67] op_sel_hi:[1,0] neg_lo:[0,1] neg_hi:[0,1]
	v_pk_add_f32 v[46:47], v[46:47], v[66:67] op_sel_hi:[1,0] neg_lo:[0,1] neg_hi:[0,1]
	v_pk_add_f32 v[48:49], v[48:49], v[66:67] op_sel_hi:[1,0] neg_lo:[0,1] neg_hi:[0,1]
	v_pk_add_f32 v[50:51], v[50:51], v[66:67] op_sel_hi:[1,0] neg_lo:[0,1] neg_hi:[0,1]
	v_pk_add_f32 v[52:53], v[52:53], v[66:67] op_sel_hi:[1,0] neg_lo:[0,1] neg_hi:[0,1]
	v_pk_add_f32 v[54:55], v[54:55], v[66:67] op_sel_hi:[1,0] neg_lo:[0,1] neg_hi:[0,1]
	v_pk_add_f32 v[56:57], v[56:57], v[66:67] op_sel_hi:[1,0] neg_lo:[0,1] neg_hi:[0,1]
	v_pk_add_f32 v[58:59], v[58:59], v[66:67] op_sel_hi:[1,0] neg_lo:[0,1] neg_hi:[0,1]
	v_pk_add_f32 v[60:61], v[60:61], v[66:67] op_sel_hi:[1,0] neg_lo:[0,1] neg_hi:[0,1]
	v_pk_add_f32 v[62:63], v[62:63], v[66:67] op_sel_hi:[1,0] neg_lo:[0,1] neg_hi:[0,1]
	v_pk_add_f32 v[64:65], v[64:65], v[66:67] op_sel_hi:[1,0] neg_lo:[0,1] neg_hi:[0,1]
	v_pk_add_f32 v[82:83], v[82:83], v[66:67] op_sel_hi:[1,0] neg_lo:[0,1] neg_hi:[0,1]
	v_pk_add_f32 v[84:85], v[84:85], v[66:67] op_sel_hi:[1,0] neg_lo:[0,1] neg_hi:[0,1]
	v_pk_add_f32 v[86:87], v[86:87], v[66:67] op_sel_hi:[1,0] neg_lo:[0,1] neg_hi:[0,1]
	v_pk_add_f32 v[88:89], v[88:89], v[66:67] op_sel_hi:[1,0] neg_lo:[0,1] neg_hi:[0,1]
	v_pk_add_f32 v[90:91], v[90:91], v[66:67] op_sel_hi:[1,0] neg_lo:[0,1] neg_hi:[0,1]
	v_pk_add_f32 v[92:93], v[92:93], v[66:67] op_sel_hi:[1,0] neg_lo:[0,1] neg_hi:[0,1]
	v_pk_add_f32 v[94:95], v[94:95], v[66:67] op_sel_hi:[1,0] neg_lo:[0,1] neg_hi:[0,1]
	v_pk_add_f32 v[96:97], v[96:97], v[66:67] op_sel_hi:[1,0] neg_lo:[0,1] neg_hi:[0,1]
	v_sub_f32_e32 v32, v32, v66
	v_sub_f32_e32 v70, v70, v66
	v_exp_f32_e32 v33, v97
	v_exp_f32_e32 v18, v18
	v_exp_f32_e32 v19, v19
	v_exp_f32_e32 v20, v20
	v_mov_b32_e32 v244, 0
	v_mov_b32_e32 v245, 0
	v_add_f32_e32 v244, v33, v244
	v_exp_f32_e32 v21, v21
	v_exp_f32_e32 v22, v22
	v_pk_add_f32 v[244:245], v[18:19], v[244:245]
	v_exp_f32_e32 v23, v23
	v_exp_f32_e32 v24, v24
	v_pk_add_f32 v[244:245], v[20:21], v[244:245]
	v_exp_f32_e32 v119, v25
	v_exp_f32_e32 v120, v26
	v_pk_add_f32 v[244:245], v[22:23], v[244:245]
	v_exp_f32_e32 v121, v27
	v_add_f32_e32 v244, v24, v244
	v_exp_f32_e32 v122, v28
	v_add_f32_e32 v244, v119, v244
	v_exp_f32_e32 v123, v29
	v_exp_f32_e32 v124, v31
	v_pk_add_f32 v[244:245], v[120:121], v[244:245]
	v_exp_f32_e32 v125, v32
	v_exp_f32_e32 v126, v30
	v_pk_add_f32 v[244:245], v[122:123], v[244:245]
	v_exp_f32_e32 v103, v2
	v_exp_f32_e32 v106, v3
	v_pk_add_f32 v[244:245], v[124:125], v[244:245]
	v_exp_f32_e32 v107, v4
	v_add_f32_e32 v244, v126, v244
	v_exp_f32_e32 v110, v5
	v_exp_f32_e32 v111, v6
	v_exp_f32_e32 v114, v7
	v_pk_add_f32 v[244:245], v[106:107], v[244:245]
	v_exp_f32_e32 v115, v8
	v_exp_f32_e32 v117, v9
	v_pk_add_f32 v[244:245], v[110:111], v[244:245]
	v_exp_f32_e32 v102, v10
	v_exp_f32_e32 v104, v11
	v_pk_add_f32 v[244:245], v[114:115], v[244:245]
	v_exp_f32_e32 v105, v12
	v_exp_f32_e32 v108, v13
	v_pk_add_f32 v[244:245], v[102:103], v[244:245]
	v_exp_f32_e32 v109, v14
	v_exp_f32_e32 v112, v15
	v_pk_add_f32 v[244:245], v[104:105], v[244:245]
	v_exp_f32_e32 v113, v16
	v_exp_f32_e32 v116, v17
	v_pk_add_f32 v[244:245], v[108:109], v[244:245]
	v_exp_f32_e32 v72, v34
	v_exp_f32_e32 v75, v35
	v_pk_add_f32 v[244:245], v[112:113], v[244:245]
	v_exp_f32_e32 v76, v36
	v_pk_add_f32 v[244:245], v[116:117], v[244:245]
	v_exp_f32_e32 v79, v37
	v_exp_f32_e32 v80, v38
	v_exp_f32_e32 v98, v39
	v_exp_f32_e32 v99, v40
	v_exp_f32_e32 v101, v41
	v_exp_f32_e32 v71, v42
	v_exp_f32_e32 v73, v43
	v_pk_add_f32 v[244:245], v[98:99], v[244:245]
	v_exp_f32_e32 v74, v44
	v_exp_f32_e32 v77, v45
	v_exp_f32_e32 v78, v46
	v_pk_add_f32 v[244:245], v[72:73], v[244:245]
	v_exp_f32_e32 v81, v47
	v_pk_add_f32 v[244:245], v[74:75], v[244:245]
	v_exp_f32_e32 v97, v48
	v_pk_add_f32 v[244:245], v[76:77], v[244:245]
	v_exp_f32_e32 v100, v49
	v_pk_add_f32 v[244:245], v[78:79], v[244:245]
	v_exp_f32_e32 v41, v50
	v_pk_add_f32 v[244:245], v[80:81], v[244:245]
	v_exp_f32_e32 v46, v51
	v_add_f32_e32 v244, v97, v244
	v_exp_f32_e32 v47, v52
	v_pk_add_f32 v[244:245], v[100:101], v[244:245]
	v_exp_f32_e32 v53, v53
	v_exp_f32_e32 v54, v54
	v_exp_f32_e32 v67, v55
	v_pk_add_f32 v[244:245], v[46:47], v[244:245]
	v_exp_f32_e32 v68, v56
	v_exp_f32_e32 v69, v57
	v_exp_f32_e32 v38, v58
	v_add_f32_e32 v244, v67, v244
	v_exp_f32_e32 v44, v59
	v_exp_f32_e32 v45, v60
	v_pk_add_f32 v[244:245], v[68:69], v[244:245]
	v_exp_f32_e32 v51, v61
	v_exp_f32_e32 v52, v62
	v_exp_f32_e32 v57, v63
	v_pk_add_f32 v[244:245], v[44:45], v[244:245]
	v_exp_f32_e32 v58, v64
	v_exp_f32_e32 v62, v65
	v_pk_add_f32 v[244:245], v[52:53], v[244:245]
	v_exp_f32_e32 v37, v82
	v_exp_f32_e32 v42, v83
	v_add_f32_e32 v244, v58, v244
	v_exp_f32_e32 v43, v84
	v_exp_f32_e32 v49, v85
	v_exp_f32_e32 v50, v86
	v_exp_f32_e32 v55, v87
	v_pk_add_f32 v[244:245], v[42:43], v[244:245]
	v_exp_f32_e32 v56, v88
	v_exp_f32_e32 v61, v89
	v_pk_add_f32 v[244:245], v[50:51], v[244:245]
	v_exp_f32_e32 v36, v90
	v_pk_add_f32 v[244:245], v[54:55], v[244:245]
	v_exp_f32_e32 v39, v91
	v_pk_add_f32 v[244:245], v[56:57], v[244:245]
	v_exp_f32_e32 v40, v92
	v_add_f32_e32 v244, v61, v244
	v_pk_add_f32 v[244:245], v[36:37], v[244:245]
	v_pk_add_f32 v[244:245], v[38:39], v[244:245]
	v_pk_add_f32 v[244:245], v[40:41], v[244:245]
	v_exp_f32_e32 v48, v93
	v_cvt_pk_bf16_f32 v2, v33, v18
	v_cvt_pk_bf16_f32 v3, v19, v20
	v_cvt_pk_bf16_f32 v4, v21, v22
	v_cvt_pk_bf16_f32 v5, v23, v24
	s_bitcmp1_b32 s96, 0
	s_cbranch_scc1 .Latt_b3m
	s_waitcnt vmcnt(0)
.Latt_b3m:
	s_waitcnt vmcnt(12)
	s_barrier
	ds_read_b64_tr_b16 v[228:229], v195
	ds_read_b64_tr_b16 v[230:231], v195 offset:1024
	ds_read_b64_tr_b16 v[232:233], v196
	ds_read_b64_tr_b16 v[234:235], v196 offset:1024
	s_waitcnt lgkmcnt(0)
	ds_read_b64_tr_b16 v[236:237], v197
	ds_read_b64_tr_b16 v[238:239], v197 offset:1024
	ds_read_b64_tr_b16 v[240:241], v198
	ds_read_b64_tr_b16 v[242:243], v198 offset:1024
	s_nop 0
	v_pk_add_f32 v[244:245], v[48:49], v[244:245]
	v_mfma_f32_32x32x16_bf16 v[18:33], v[228:231], v[2:5], 0
	v_exp_f32_e32 v63, v94
	v_exp_f32_e32 v65, v95
	v_exp_f32_e32 v64, v96
	v_mfma_f32_32x32x16_bf16 v[2:17], v[232:235], v[2:5], 0
	v_exp_f32_e32 v70, v70
	v_pk_add_f32 v[244:245], v[62:63], v[244:245]
	v_cvt_pk_bf16_f32 v82, v119, v120
	v_cvt_pk_bf16_f32 v83, v121, v122
	v_cvt_pk_bf16_f32 v84, v123, v124
	v_cvt_pk_bf16_f32 v85, v125, v126
	s_waitcnt lgkmcnt(0)
	ds_read_b64_tr_b16 v[228:229], v199
	ds_read_b64_tr_b16 v[230:231], v199 offset:1024
	ds_read_b64_tr_b16 v[232:233], v200
	ds_read_b64_tr_b16 v[234:235], v200 offset:1024
	v_mfma_f32_32x32x16_bf16 v[18:33], v[236:239], v[82:85], v[18:33]
	v_pk_add_f32 v[244:245], v[64:65], v[244:245]
	v_pk_add_f32 v[244:245], v[70:71], v[244:245]
	v_add_f32_e32 v59, v244, v245
	v_mov_b32_e32 v60, v59
	s_nop 1
	v_permlane32_swap_b32_e32 v60, v59
	v_mfma_f32_32x32x16_bf16 v[2:17], v[240:243], v[82:85], v[2:17]
